# baseline (speedup 1.0000x reference)
_Z11main_kernelPKDv8_DF16bS1_PKfS3_S3_PKiPKtS3_S3_Pf:
	s_lshl_b32 s14, s2, 5
	s_load_dwordx4 s[4:7], s[0:1], 0x0
	s_load_dwordx2 s[36:37], s[0:1], 0x10
	s_load_dwordx4 s[8:11], s[0:1], 0x28
	s_and_b32 s3, s14, 0xe0
	s_lshr_b32 s33, s2, 3
	s_or_b32 s15, s3, s33
	v_lshrrev_b32_e32 v73, 6, v0
	s_lshl_b32 s34, s15, 3
	v_or_b32_e32 v54, s34, v73
	v_mov_b32_e32 v55, 0
	v_and_b32_e32 v1, 63, v0
	v_lshlrev_b64 v[188:189], 7, v[54:55]
	s_waitcnt lgkmcnt(0)
	v_lshl_add_u64 v[188:189], s[10:11], 0, v[188:189]
	v_lshlrev_b32_e32 v4, 1, v1
	v_mov_b32_e32 v5, v55
	v_lshl_add_u64 v[188:189], v[188:189], 0, v[4:5]
	v_and_b32_e32 v2, 7, v0
	v_bfe_u32 v74, v0, 4, 2
	v_lshlrev_b32_e32 v2, 4, v2
	s_mov_b32 s13, 0
	s_lshl_b32 s2, s15, 1
	s_lshl_b32 s12, s15, 2
	v_lshl_or_b32 v2, v74, 7, v2
	v_mov_b32_e32 v3, v55
	s_and_b32 s10, s2, 0x3ffffffc
	v_lshl_add_u64 v[58:59], s[4:5], 0, v[2:3]
	s_lshl_b64 s[2:3], s[12:13], 9
	v_lshl_add_u64 v[2:3], v[58:59], 0, s[2:3]
	s_or_b32 s2, s12, 1
	s_mov_b32 s3, s13
	s_lshl_b64 s[2:3], s[2:3], 9
	v_lshl_add_u64 v[4:5], v[58:59], 0, s[2:3]
	s_or_b32 s2, s12, 2
	s_mov_b32 s3, s13
	s_lshl_b64 s[2:3], s[2:3], 9
	global_load_dwordx4 v[22:25], v[2:3], off
	global_load_dwordx4 v[50:53], v[4:5], off
	v_lshl_add_u64 v[2:3], v[58:59], 0, s[2:3]
	s_or_b32 s2, s12, 3
	s_mov_b32 s3, s13
	s_lshl_b64 s[2:3], s[2:3], 9
	v_lshl_add_u64 v[4:5], v[58:59], 0, s[2:3]
	s_and_b32 s2, s14, 0x700
	s_add_i32 s5, s33, 1
	s_lshl_b32 s14, s2, 4
	s_lshl_b32 s2, s5, 8
	s_and_b32 s2, s2, 0x700
	s_add_i32 s38, s33, 2
	s_lshl_b32 s16, s2, 4
	s_lshl_b32 s2, s38, 8
	s_and_b32 s2, s2, 0x700
	s_add_i32 s39, s33, 3
	s_lshl_b32 s18, s2, 4
	s_lshl_b32 s2, s39, 8
	s_and_b32 s44, s15, 0x1fffff80
	v_lshlrev_b32_e32 v75, 3, v73
	s_and_b32 s2, s2, 0x700
	s_add_i32 s40, s33, 4
	global_load_dwordx4 v[60:63], v[2:3], off
	global_load_dwordx4 v[64:67], v[4:5], off
	v_or_b32_e32 v2, s44, v75
	v_mov_b32_e32 v3, v55
	s_lshl_b32 s20, s2, 4
	s_lshl_b32 s2, s40, 8
	v_lshlrev_b64 v[2:3], 12, v[2:3]
	s_and_b32 s2, s2, 0x700
	s_add_i32 s41, s33, 5
	v_lshl_add_u64 v[2:3], s[6:7], 0, v[2:3]
	v_lshlrev_b32_e32 v56, 4, v1
	v_mov_b32_e32 v57, v55
	s_lshl_b32 s22, s2, 4
	s_lshl_b32 s2, s41, 8
	v_lshl_add_u64 v[2:3], v[2:3], 0, v[56:57]
	s_mov_b32 s15, s13
	s_and_b32 s2, s2, 0x700
	s_add_i32 s42, s33, 6
	v_lshl_add_u64 v[4:5], v[2:3], 0, s[14:15]
	s_mov_b32 s17, s13
	s_lshl_b32 s24, s2, 4
	s_lshl_b32 s2, s42, 8
	global_load_dwordx4 v[18:21], v[4:5], off
	global_load_dwordx4 v[26:29], v[4:5], off offset:1024
	global_load_dwordx4 v[30:33], v[4:5], off offset:2048
	global_load_dwordx4 v[34:37], v[4:5], off offset:3072
	v_lshl_add_u64 v[4:5], v[2:3], 0, s[16:17]
	s_mov_b32 s19, s13
	s_and_b32 s2, s2, 0x700
	s_add_i32 s43, s33, 7
	global_load_dwordx4 v[38:41], v[4:5], off
	global_load_dwordx4 v[42:45], v[4:5], off offset:1024
	global_load_dwordx4 v[68:71], v[4:5], off offset:2048
	global_load_dwordx4 v[76:79], v[4:5], off offset:3072
	v_lshl_add_u64 v[4:5], v[2:3], 0, s[18:19]
	s_mov_b32 s21, s13
	s_lshl_b32 s26, s2, 4
	s_lshl_b32 s2, s43, 8
	global_load_dwordx4 v[80:83], v[4:5], off
	global_load_dwordx4 v[84:87], v[4:5], off offset:1024
	global_load_dwordx4 v[88:91], v[4:5], off offset:2048
	global_load_dwordx4 v[92:95], v[4:5], off offset:3072
	v_lshl_add_u64 v[4:5], v[2:3], 0, s[20:21]
	s_mov_b32 s23, s13
	s_and_b32 s2, s2, 0x700
	s_and_b32 s30, s34, 0x7ffffc00
	s_mov_b32 s31, s13
	global_load_dwordx4 v[96:99], v[4:5], off
	global_load_dwordx4 v[100:103], v[4:5], off offset:1024
	global_load_dwordx4 v[104:107], v[4:5], off offset:2048
	global_load_dwordx4 v[108:111], v[4:5], off offset:3072
	v_lshl_add_u64 v[4:5], v[2:3], 0, s[22:23]
	s_mov_b32 s25, s13
	s_lshl_b32 s28, s2, 4
	s_lshl_b64 s[2:3], s[30:31], 2
	global_load_dwordx4 v[112:115], v[4:5], off
	global_load_dwordx4 v[116:119], v[4:5], off offset:1024
	global_load_dwordx4 v[120:123], v[4:5], off offset:2048
	global_load_dwordx4 v[124:127], v[4:5], off offset:3072
	v_lshl_add_u64 v[4:5], v[2:3], 0, s[24:25]
	s_mov_b32 s27, s13
	s_mov_b32 s29, s13
	s_add_u32 s2, s36, s2
	global_load_dwordx4 v[128:131], v[4:5], off
	global_load_dwordx4 v[132:135], v[4:5], off offset:1024
	global_load_dwordx4 v[136:139], v[4:5], off offset:2048
	global_load_dwordx4 v[140:143], v[4:5], off offset:3072
	v_lshl_add_u64 v[4:5], v[2:3], 0, s[26:27]
	v_lshl_add_u64 v[2:3], v[2:3], 0, s[28:29]
	s_addc_u32 s3, s37, s3
	global_load_dwordx4 v[144:147], v[4:5], off
	global_load_dwordx4 v[148:151], v[4:5], off offset:1024
	global_load_dwordx4 v[152:155], v[4:5], off offset:2048
	global_load_dwordx4 v[156:159], v[4:5], off offset:3072
	global_load_dwordx4 v[160:163], v[2:3], off
	global_load_dwordx4 v[164:167], v[2:3], off offset:1024
	global_load_dwordx4 v[168:171], v[2:3], off offset:2048
	global_load_dwordx4 v[172:175], v[2:3], off offset:3072
	global_load_dwordx4 v[14:17], v56, s[2:3]
	global_load_dwordx4 v[10:13], v56, s[2:3] offset:1024
	global_load_dwordx4 v[6:9], v56, s[2:3] offset:2048
	s_nop 0
	global_load_dwordx4 v[2:5], v56, s[2:3] offset:3072
	global_load_ushort v72, v[188:189], off
	s_load_dwordx2 s[2:3], s[0:1], 0x40
	s_load_dword s15, s[8:9], s10 offset:0x0
	v_lshlrev_b32_e32 v1, 2, v1
	s_waitcnt lgkmcnt(0)
	s_load_dword s4, s[2:3], 0x0
	s_cmp_lg_u32 s15, 1
	s_cbranch_scc1 .Lmy_generic
	s_load_dwordx2 s[0:1], s[0:1], 0x48
	s_mov_b64 s[2:3], -1
	v_lshlrev_b32_e32 v176, 9, v73
	s_movk_i32 s6, 0x4040
	v_and_b32_e32 v177, 15, v0
	v_mad_u32_u24 v176, v74, s6, v176
	v_lshl_or_b32 v176, v177, 2, v176
	s_lshl_b32 s6, s33, 6
	s_and_b32 s6, s6, 0x1c0
	v_add_u32_e32 v177, s6, v176
	s_lshl_b32 s6, s5, 6
	s_and_b32 s6, s6, 0x1c0
	v_add_u32_e32 v178, s6, v176
	s_lshl_b32 s6, s38, 6
	s_and_b32 s6, s6, 0x1c0
	v_add_u32_e32 v179, s6, v176
	s_lshl_b32 s6, s39, 6
	s_and_b32 s6, s6, 0x1c0
	v_add_u32_e32 v180, s6, v176
	s_lshl_b32 s6, s40, 6
	s_and_b32 s6, s6, 0x1c0
	v_add_u32_e32 v181, s6, v176
	s_lshl_b32 s6, s41, 6
	s_and_b32 s6, s6, 0x1c0
	v_add_u32_e32 v182, s6, v176
	s_lshl_b32 s6, s42, 6
	s_and_b32 s6, s6, 0x1c0
	v_add_u32_e32 v183, s6, v176
	s_lshl_b32 s6, s43, 6
	s_and_b32 s6, s6, 0x1c0
	v_add_u32_e32 v184, s6, v176
	s_waitcnt vmcnt(36)
	v_mfma_f32_16x16x32_bf16 v[18:21], v[22:25], v[18:21], 0
	s_waitcnt vmcnt(35)
	v_mfma_f32_16x16x32_bf16 v[18:21], v[50:53], v[26:29], v[18:21]
	s_waitcnt vmcnt(34)
	v_mfma_f32_16x16x32_bf16 v[18:21], v[60:63], v[30:33], v[18:21]
	s_waitcnt vmcnt(33)
	v_mfma_f32_16x16x32_bf16 v[46:49], v[64:67], v[34:37], v[18:21]
	s_waitcnt vmcnt(32)
	v_mfma_f32_16x16x32_bf16 v[18:21], v[22:25], v[38:41], 0
	s_waitcnt vmcnt(31)
	v_mfma_f32_16x16x32_bf16 v[18:21], v[50:53], v[42:45], v[18:21]
	s_waitcnt vmcnt(30)
	v_mfma_f32_16x16x32_bf16 v[18:21], v[60:63], v[68:71], v[18:21]
	s_waitcnt vmcnt(29)
	v_mfma_f32_16x16x32_bf16 v[42:45], v[64:67], v[76:79], v[18:21]
	ds_write_b32 v177, v46
	ds_write_b32 v177, v47 offset:4112
	ds_write_b32 v177, v48 offset:8224
	ds_write_b32 v177, v49 offset:12336
	s_waitcnt vmcnt(28)
	v_mfma_f32_16x16x32_bf16 v[18:21], v[22:25], v[80:83], 0
	s_waitcnt vmcnt(27)
	v_mfma_f32_16x16x32_bf16 v[18:21], v[50:53], v[84:87], v[18:21]
	s_waitcnt vmcnt(26)
	v_mfma_f32_16x16x32_bf16 v[18:21], v[60:63], v[88:91], v[18:21]
	s_waitcnt vmcnt(25)
	v_mfma_f32_16x16x32_bf16 v[38:41], v[64:67], v[92:95], v[18:21]
	ds_write_b32 v178, v42
	ds_write_b32 v178, v43 offset:4112
	ds_write_b32 v178, v44 offset:8224
	ds_write_b32 v178, v45 offset:12336
	s_waitcnt vmcnt(24)
	v_mfma_f32_16x16x32_bf16 v[18:21], v[22:25], v[96:99], 0
	s_waitcnt vmcnt(23)
	v_mfma_f32_16x16x32_bf16 v[18:21], v[50:53], v[100:103], v[18:21]
	s_waitcnt vmcnt(22)
	v_mfma_f32_16x16x32_bf16 v[18:21], v[60:63], v[104:107], v[18:21]
	s_waitcnt vmcnt(21)
	v_mfma_f32_16x16x32_bf16 v[34:37], v[64:67], v[108:111], v[18:21]
	ds_write_b32 v179, v38
	ds_write_b32 v179, v39 offset:4112
	ds_write_b32 v179, v40 offset:8224
	ds_write_b32 v179, v41 offset:12336
	s_waitcnt vmcnt(20)
	v_mfma_f32_16x16x32_bf16 v[18:21], v[22:25], v[112:115], 0
	s_waitcnt vmcnt(19)
	v_mfma_f32_16x16x32_bf16 v[18:21], v[50:53], v[116:119], v[18:21]
	s_waitcnt vmcnt(18)
	v_mfma_f32_16x16x32_bf16 v[18:21], v[60:63], v[120:123], v[18:21]
	s_waitcnt vmcnt(17)
	v_mfma_f32_16x16x32_bf16 v[30:33], v[64:67], v[124:127], v[18:21]
	ds_write_b32 v180, v34
	ds_write_b32 v180, v35 offset:4112
	ds_write_b32 v180, v36 offset:8224
	ds_write_b32 v180, v37 offset:12336
	s_waitcnt vmcnt(16)
	v_mfma_f32_16x16x32_bf16 v[18:21], v[22:25], v[128:131], 0
	s_waitcnt vmcnt(15)
	v_mfma_f32_16x16x32_bf16 v[18:21], v[50:53], v[132:135], v[18:21]
	s_waitcnt vmcnt(14)
	v_mfma_f32_16x16x32_bf16 v[18:21], v[60:63], v[136:139], v[18:21]
	s_waitcnt vmcnt(13)
	v_mfma_f32_16x16x32_bf16 v[26:29], v[64:67], v[140:143], v[18:21]
	ds_write_b32 v181, v30
	ds_write_b32 v181, v31 offset:4112
	ds_write_b32 v181, v32 offset:8224
	ds_write_b32 v181, v33 offset:12336
	s_waitcnt vmcnt(12)
	v_mfma_f32_16x16x32_bf16 v[18:21], v[22:25], v[144:147], 0
	s_waitcnt vmcnt(8)
	v_mfma_f32_16x16x32_bf16 v[22:25], v[22:25], v[160:163], 0
	v_mfma_f32_16x16x32_bf16 v[18:21], v[50:53], v[148:151], v[18:21]
	s_waitcnt vmcnt(7)
	v_mfma_f32_16x16x32_bf16 v[22:25], v[50:53], v[164:167], v[22:25]
	v_mfma_f32_16x16x32_bf16 v[18:21], v[60:63], v[152:155], v[18:21]
	s_waitcnt vmcnt(6)
	v_mfma_f32_16x16x32_bf16 v[22:25], v[60:63], v[168:171], v[22:25]
	ds_write_b32 v182, v26
	ds_write_b32 v182, v27 offset:4112
	ds_write_b32 v182, v28 offset:8224
	ds_write_b32 v182, v29 offset:12336
	v_mfma_f32_16x16x32_bf16 v[18:21], v[64:67], v[156:159], v[18:21]
	s_waitcnt vmcnt(5)
	v_mfma_f32_16x16x32_bf16 v[22:25], v[64:67], v[172:175], v[22:25]
	s_nop 7
	ds_write_b32 v183, v18
	ds_write_b32 v183, v19 offset:4112
	ds_write_b32 v183, v20 offset:8224
	ds_write_b32 v183, v21 offset:12336
	ds_write_b32 v184, v22
	ds_write_b32 v184, v23 offset:4112
	ds_write_b32 v184, v24 offset:8224
	ds_write_b32 v184, v25 offset:12336
	s_branch .LBB1_4
